# sfirst
# speedup vs baseline: 1.0082x; 1.0082x over previous
_Z11attn_kernelILi4EEvPKfS1_S1_S1_S1_S1_PKcPf:
	s_load_dwordx2 s[24:25], s[0:1], 0x30
	s_load_dwordx8 s[8:15], s[0:1], 0x0
	s_load_dwordx4 s[16:19], s[0:1], 0x20
	v_lshrrev_b32_e32 v63, 6, v0
	v_and_b32_e32 v57, 15, v0
	v_bfe_u32 v1, v0, 4, 2
	v_lshrrev_b32_e32 v2, 2, v57
	v_mul_u32_u24_e32 v4, 3, v1
	v_mul_u32_u24_e32 v2, 3, v2
	v_mad_u32_u24 v4, v63, 12, v4
	v_mad_u32_u24 v2, v63, 12, v2
	v_lshlrev_b32_e32 v4, 2, v4
	v_lshlrev_b32_e32 v2, 2, v2
	v_and_b32_e32 v104, 63, v0
	v_lshlrev_b32_e32 v60, 5, v57
	v_lshlrev_b32_e32 v58, 3, v1
	v_add_u32_e32 v3, v60, v58
	v_lshrrev_b32_e32 v56, 4, v0
	v_lshlrev_b32_e32 v54, 4, v57
	v_mov_b32_e32 v59, 0
	s_movk_i32 s4, 0xe0
	v_cmp_gt_u32_e64 s[4:5], s4, v0
	s_lshl_b32 s26, s2, 8
	s_lshl_b32 s27, s2, 9
	s_mul_i32 s28, s2, 14
	s_add_u32 s26, s26, 0x164000
	s_add_u32 s27, s27, 0x80000
	s_add_u32 s20, s26, 0xc0
	v_lshlrev_b32_e32 v5, 2, v57
	v_lshlrev_b32_e32 v147, 6, v57
	v_add_u32_e32 v2, s26, v2
	v_add_u32_e32 v4, s26, v4
	v_add_u32_e32 v3, s27, v3
	v_mul_u32_u24_e32 v156, 0x140, v1
	s_movk_i32 s21, 0x500
	v_mad_u32_u24 v156, v63, s21, v156
	v_lshl_or_b32 v156, v57, 2, v156
	v_add_u32_e32 v156, 0x1c00, v156
	v_lshlrev_b32_e32 v157, 5, v56
	v_cmp_gt_u32_e32 vcc, 3, v57
	v_add_u32_e32 v158, 4, v57
	v_lshlrev_b32_e32 v159, 2, v57
	s_movk_i32 s21, 0x50
	v_cndmask_b32_e32 v158, 4, v158, vcc
	v_mad_u32_u24 v159, v56, s21, v159
	v_lshl_add_u32 v158, v158, 2, v157
	v_mul_u32_u24_e32 v250, 0x50, v56
	v_or_b32_e32 v250, 0x3800, v250
	v_lshl_add_u32 v251, v57, 1, v250
	v_mul_u32_u24_e32 v252, 0x50, v57
	v_lshl_add_u32 v252, v58, 1, v252
	v_lshlrev_b32_e32 v253, 2, v57
	v_and_b32_e32 v254, 0xc0, v0
	v_lshlrev_b32_e32 v255, 11, v1
	v_or3_b32 v253, v253, v254, v255
	v_add_u32_e32 v254, s28, v56
	v_lshl_add_u32 v254, v254, 9, v54
	v_lshl_or_b32 v255, v56, 9, v54
	s_waitcnt lgkmcnt(0)
	s_load_dword s3, s[24:25], s20
	global_load_dwordx3 v[80:82], v2, s[24:25]
	global_load_dwordx3 v[84:86], v4, s[24:25]
	global_load_dwordx2 v[64:65], v3, s[24:25]
	s_add_u32 s22, s24, 0x160000
	s_addc_u32 s23, s25, 0
	v_cndmask_b32_e64 v62, 13, v56, s[4:5]
	v_add_u32_e32 v3, s28, v62
	v_mad_u32_u24 v144, v3, 36, v5
	v_mad_u32_u24 v146, v3, 12, v5
	v_add_u32_e32 v145, -36, v146
	v_add_u32_e32 v146, -48, v146
	v_lshl_or_b32 v147, v63, 10, v147
	v_lshl_or_b32 v147, v1, 4, v147
	v_or_b32_e32 v148, 0x1000, v147
	v_lshlrev_b32_e32 v149, 4, v104
	v_lshlrev_b32_e32 v150, 9, v3
	v_add_u32_e32 v150, v150, v54
	v_and_b32_e32 v87, 3, v57
	v_lshlrev_b32_e32 v87, 4, v87
	v_lshl_or_b32 v87, v1, 6, v87
	v_lshlrev_b32_e32 v88, 3, v57
	s_add_u32 s26, s24, 0x100000
	s_addc_u32 s27, s25, 0
	s_add_u32 s28, s24, 0x140000
	s_addc_u32 s29, s25, 0
	s_movk_i32 s6, 0x140
	v_cmp_gt_u32_e32 vcc, s6, v0
	v_lshlrev_b32_e32 v22, 2, v0
	v_mov_b32_e32 v23, 0
	s_and_saveexec_b64 s[6:7], vcc
	ds_write_b32 v22, v23 offset:14336
	s_or_b64 exec, exec, s[6:7]
	v_cmp_gt_u32_e32 vcc, 64, v0
	s_and_saveexec_b64 s[6:7], vcc
	ds_write_b32 v22, v23 offset:15360
	s_or_b64 exec, exec, s[6:7]
	v_mov_b32_e32 v45, 0xc9c35000
	s_mov_b32 s30, 0x3db8aa3b
	s_mov_b32 s31, 0x3db8aa3b
	v_mov_b32_e32 v121, 0x3fb8aa3b
	v_mov_b32_e32 v35, 0
	v_mov_b32_e32 v44, v45
	s_waitcnt lgkmcnt(0)
	s_bitcmp0_b32 s3, 1
	s_cselect_b64 s[20:21], -1, 0
	s_cbranch_scc1 .LBB1_16
	v_bfe_u32 v46, s3, v57, 1
	v_cmp_eq_u32_e32 vcc, 0, v46
	s_nop 1
	v_cndmask_b32_e32 v47, 0, v45, vcc
	v_cndmask_b32_e64 v55, 1.0, 0, vcc
	s_nop 0
	v_mov_b32_dpp v34, v47 row_newbcast:0 row_mask:0xf bank_mask:0xf bound_ctrl:1
	v_mov_b32_dpp v36, v47 row_newbcast:2 row_mask:0xf bank_mask:0xf bound_ctrl:1
	v_mov_b32_dpp v37, v47 row_newbcast:3 row_mask:0xf bank_mask:0xf bound_ctrl:1
	v_mov_b32_dpp v22, v47 row_newbcast:4 row_mask:0xf bank_mask:0xf bound_ctrl:1
	v_mov_b32_dpp v23, v47 row_newbcast:5 row_mask:0xf bank_mask:0xf bound_ctrl:1
	v_mov_b32_dpp v24, v47 row_newbcast:6 row_mask:0xf bank_mask:0xf bound_ctrl:1
	v_mov_b32_dpp v25, v47 row_newbcast:7 row_mask:0xf bank_mask:0xf bound_ctrl:1
	v_mov_b32_dpp v38, v47 row_newbcast:8 row_mask:0xf bank_mask:0xf bound_ctrl:1
	v_mov_b32_dpp v39, v47 row_newbcast:9 row_mask:0xf bank_mask:0xf bound_ctrl:1
	v_mov_b32_dpp v40, v47 row_newbcast:10 row_mask:0xf bank_mask:0xf bound_ctrl:1
	v_mov_b32_dpp v41, v47 row_newbcast:11 row_mask:0xf bank_mask:0xf bound_ctrl:1
	v_mov_b32_dpp v42, v47 row_newbcast:12 row_mask:0xf bank_mask:0xf bound_ctrl:1
	v_mov_b32_dpp v43, v47 row_newbcast:13 row_mask:0xf bank_mask:0xf bound_ctrl:1
	s_waitcnt vmcnt(1)
	v_lshl_add_u32 v72, v80, 9, v87
	v_lshl_add_u32 v73, v81, 9, v87
	v_lshl_add_u32 v74, v82, 9, v87
	global_load_dwordx4 v[50:53], v72, s[24:25]
	global_load_dwordx4 v[46:49], v72, s[24:25] offset:256
	global_load_dwordx4 v[14:17], v73, s[24:25]
	global_load_dwordx4 v[10:13], v73, s[24:25] offset:256
	global_load_dwordx4 v[6:9], v74, s[24:25]
	global_load_dwordx4 v[2:5], v74, s[24:25] offset:256
	v_lshl_add_u32 v75, v84, 8, v54
	v_lshl_add_u32 v78, v84, 7, v88
	v_lshl_add_u32 v76, v85, 8, v54
	v_lshl_add_u32 v79, v85, 7, v88
	v_lshl_add_u32 v77, v86, 8, v54
	v_lshl_add_u32 v80, v86, 7, v88
	global_load_dwordx4 v[30:33], v75, s[26:27]
	global_load_dwordx2 v[70:71], v78, s[28:29]
	global_load_dwordx4 v[26:29], v76, s[26:27]
	global_load_dwordx2 v[66:67], v79, s[28:29]
	global_load_dwordx4 v[18:21], v77, s[26:27]
	global_load_dwordx2 v[68:69], v80, s[28:29]
	s_mov_b32 exec_lo, 0x1ff01ff
	s_mov_b32 exec_hi, 0x1ff01ff
	global_load_dword v120, v144, s[10:11]
	s_mov_b32 exec_lo, 0xe000e00
	s_mov_b32 exec_hi, 0xe000e00
	global_load_dword v120, v145, s[12:13]
	s_mov_b32 exec_lo, 0x70007000
	s_mov_b32 exec_hi, 0x70007000
	global_load_dword v120, v146, s[14:15]
	s_mov_b64 exec, -1
	global_load_dwordx4 v[124:127], v147, s[22:23]
	global_load_dwordx4 v[128:131], v148, s[22:23]
	s_mov_b32 exec_hi, 0
	global_load_dwordx4 v[132:135], v149, s[16:17]
	s_mov_b32 exec_hi, -1
	s_mov_b32 exec_lo, 0
	global_load_dwordx4 v[132:135], v149, s[18:19] offset:-512
	s_mov_b32 exec_lo, -1
	global_load_dwordx4 v[136:139], v150, s[8:9]
	global_load_dwordx4 v[140:143], v150, s[8:9] offset:256
	v_mov_b32_e32 v75, 0
	v_mov_b32_e32 v79, 0
	v_mov_b32_e32 v83, 0
	s_waitcnt vmcnt(20)
	v_mfma_f32_16x16x32_fp8_fp8 v[160:163], v[50:51], v[64:65], v[34:37]
	v_mfma_f32_16x16x32_fp8_fp8 v[164:167], v[52:53], v[64:65], v[22:25]
	s_waitcnt vmcnt(19)
	v_mfma_f32_16x16x32_fp8_fp8 v[168:171], v[46:47], v[64:65], v[38:41]
	v_mfma_f32_16x16x32_fp8_fp8 v[172:175], v[48:49], v[64:65], v[42:45]
	s_nop 3
	v_max3_f32 v86, v160, v161, v162
	v_max3_f32 v87, v163, v164, v165
	v_max3_f32 v88, v166, v167, v168
	v_max3_f32 v89, v169, v170, v171
	v_max3_f32 v86, v86, v172, v173
	v_max3_f32 v87, v87, v88, v89
	v_max_f32_e32 v96, v86, v87
	v_mul_f32_e32 v98, 0xbdb8aa3b, v96
	v_pk_fma_f32 v[208:209], v[160:161], s[30:31], v[98:99] op_sel_hi:[1,1,0]
	v_pk_fma_f32 v[210:211], v[162:163], s[30:31], v[98:99] op_sel_hi:[1,1,0]
	v_pk_fma_f32 v[212:213], v[164:165], s[30:31], v[98:99] op_sel_hi:[1,1,0]
	v_pk_fma_f32 v[214:215], v[166:167], s[30:31], v[98:99] op_sel_hi:[1,1,0]
	v_pk_fma_f32 v[216:217], v[168:169], s[30:31], v[98:99] op_sel_hi:[1,1,0]
	v_pk_fma_f32 v[218:219], v[170:171], s[30:31], v[98:99] op_sel_hi:[1,1,0]
	v_pk_fma_f32 v[220:221], v[172:173], s[30:31], v[98:99] op_sel_hi:[1,1,0]
	v_exp_f32_e32 v208, v208
	v_exp_f32_e32 v209, v209
	v_exp_f32_e32 v210, v210
	v_exp_f32_e32 v211, v211
	v_exp_f32_e32 v212, v212
	v_exp_f32_e32 v213, v213
	v_exp_f32_e32 v214, v214
	v_exp_f32_e32 v215, v215
	v_exp_f32_e32 v216, v216
	v_exp_f32_e32 v217, v217
	v_exp_f32_e32 v218, v218
	v_exp_f32_e32 v219, v219
	v_exp_f32_e32 v220, v220
	v_exp_f32_e32 v221, v221
	s_waitcnt vmcnt(18)
	v_mfma_f32_16x16x32_fp8_fp8 v[176:179], v[14:15], v[64:65], v[34:37]
	v_mfma_f32_16x16x32_fp8_fp8 v[180:183], v[16:17], v[64:65], v[22:25]
	s_waitcnt vmcnt(17)
	v_mfma_f32_16x16x32_fp8_fp8 v[184:187], v[10:11], v[64:65], v[38:41]
	v_mfma_f32_16x16x32_fp8_fp8 v[188:191], v[12:13], v[64:65], v[42:45]
	v_pk_add_f32 v[86:87], v[208:209], v[210:211]
	v_pk_add_f32 v[88:89], v[212:213], v[214:215]
	v_pk_add_f32 v[90:91], v[216:217], v[218:219]
	v_pk_mul_f32 v[92:93], v[208:209], v[160:161]
	v_pk_mul_f32 v[94:95], v[210:211], v[162:163]
	v_pk_add_f32 v[86:87], v[86:87], v[220:221]
	v_pk_add_f32 v[88:89], v[88:89], v[90:91]
	v_pk_fma_f32 v[92:93], v[212:213], v[164:165], v[92:93]
	v_pk_fma_f32 v[94:95], v[214:215], v[166:167], v[94:95]
	v_pk_add_f32 v[86:87], v[86:87], v[88:89]
	v_pk_fma_f32 v[92:93], v[216:217], v[168:169], v[92:93]
	v_pk_fma_f32 v[94:95], v[218:219], v[170:171], v[94:95]
	v_add_f32_e32 v86, v86, v87
	v_pk_fma_f32 v[92:93], v[220:221], v[172:173], v[92:93]
	v_rcp_f32_e32 v87, v86
	v_pk_add_f32 v[92:93], v[92:93], v[94:95]
	v_mul_f32_e32 v87, v55, v87
	v_add_f32_e32 v92, v92, v93
	v_mul_f32_e32 v107, v86, v87
	v_mul_f32_e32 v92, v92, v87
	v_mul_f32_e32 v100, 0x43800000, v87
	v_mul_f32_e32 v103, 0x3d800000, v92
	v_max3_f32 v86, v176, v177, v178
	v_max3_f32 v87, v179, v180, v181
	v_max3_f32 v88, v182, v183, v184
	v_max3_f32 v89, v185, v186, v187
	v_max3_f32 v86, v86, v188, v189
	v_max3_f32 v87, v87, v88, v89
	v_max_f32_e32 v96, v86, v87
	v_mul_f32_e32 v98, 0xbdb8aa3b, v96
	v_pk_fma_f32 v[222:223], v[176:177], s[30:31], v[98:99] op_sel_hi:[1,1,0]
	v_pk_fma_f32 v[224:225], v[178:179], s[30:31], v[98:99] op_sel_hi:[1,1,0]
	v_pk_fma_f32 v[226:227], v[180:181], s[30:31], v[98:99] op_sel_hi:[1,1,0]
	v_pk_fma_f32 v[228:229], v[182:183], s[30:31], v[98:99] op_sel_hi:[1,1,0]
	v_pk_fma_f32 v[230:231], v[184:185], s[30:31], v[98:99] op_sel_hi:[1,1,0]
	v_pk_fma_f32 v[232:233], v[186:187], s[30:31], v[98:99] op_sel_hi:[1,1,0]
	v_pk_fma_f32 v[234:235], v[188:189], s[30:31], v[98:99] op_sel_hi:[1,1,0]
	v_exp_f32_e32 v222, v222
	v_exp_f32_e32 v223, v223
	v_exp_f32_e32 v224, v224
	v_exp_f32_e32 v225, v225
	v_exp_f32_e32 v226, v226
	v_exp_f32_e32 v227, v227
	v_exp_f32_e32 v228, v228
	v_exp_f32_e32 v229, v229
	v_exp_f32_e32 v230, v230
	v_exp_f32_e32 v231, v231
	v_exp_f32_e32 v232, v232
	v_exp_f32_e32 v233, v233
	v_exp_f32_e32 v234, v234
	v_exp_f32_e32 v235, v235
	s_waitcnt vmcnt(16)
	v_mfma_f32_16x16x32_fp8_fp8 v[192:195], v[6:7], v[64:65], v[34:37]
	v_mfma_f32_16x16x32_fp8_fp8 v[196:199], v[8:9], v[64:65], v[22:25]
	s_waitcnt vmcnt(15)
	v_mfma_f32_16x16x32_fp8_fp8 v[200:203], v[2:3], v[64:65], v[38:41]
	v_mfma_f32_16x16x32_fp8_fp8 v[204:207], v[4:5], v[64:65], v[42:45]
	v_pk_add_f32 v[86:87], v[222:223], v[224:225]
	v_pk_add_f32 v[88:89], v[226:227], v[228:229]
	v_pk_add_f32 v[90:91], v[230:231], v[232:233]
	v_pk_mul_f32 v[92:93], v[222:223], v[176:177]
	v_pk_mul_f32 v[94:95], v[224:225], v[178:179]
	v_pk_add_f32 v[86:87], v[86:87], v[234:235]
	v_pk_add_f32 v[88:89], v[88:89], v[90:91]
	v_pk_fma_f32 v[92:93], v[226:227], v[180:181], v[92:93]
	v_pk_fma_f32 v[94:95], v[228:229], v[182:183], v[94:95]
	v_pk_add_f32 v[86:87], v[86:87], v[88:89]
	v_pk_fma_f32 v[92:93], v[230:231], v[184:185], v[92:93]
	v_pk_fma_f32 v[94:95], v[232:233], v[186:187], v[94:95]
	v_add_f32_e32 v86, v86, v87
	v_pk_fma_f32 v[92:93], v[234:235], v[188:189], v[92:93]
	v_rcp_f32_e32 v87, v86
	v_pk_add_f32 v[92:93], v[92:93], v[94:95]
	v_mul_f32_e32 v87, v55, v87
	v_add_f32_e32 v92, v92, v93
	v_mul_f32_e32 v108, v86, v87
	v_mul_f32_e32 v92, v92, v87
	v_mul_f32_e32 v101, 0x43800000, v87
	v_mul_f32_e32 v105, 0x3d800000, v92
	v_max3_f32 v86, v192, v193, v194
	v_max3_f32 v87, v195, v196, v197
	v_max3_f32 v88, v198, v199, v200
	v_max3_f32 v89, v201, v202, v203
	v_max3_f32 v86, v86, v204, v205
	v_max3_f32 v87, v87, v88, v89
	v_max_f32_e32 v96, v86, v87
	v_mul_f32_e32 v98, 0xbdb8aa3b, v96
	v_pk_fma_f32 v[236:237], v[192:193], s[30:31], v[98:99] op_sel_hi:[1,1,0]
	v_pk_fma_f32 v[238:239], v[194:195], s[30:31], v[98:99] op_sel_hi:[1,1,0]
	v_pk_fma_f32 v[240:241], v[196:197], s[30:31], v[98:99] op_sel_hi:[1,1,0]
	v_pk_fma_f32 v[242:243], v[198:199], s[30:31], v[98:99] op_sel_hi:[1,1,0]
	v_pk_fma_f32 v[244:245], v[200:201], s[30:31], v[98:99] op_sel_hi:[1,1,0]
	v_pk_fma_f32 v[246:247], v[202:203], s[30:31], v[98:99] op_sel_hi:[1,1,0]
	v_pk_fma_f32 v[248:249], v[204:205], s[30:31], v[98:99] op_sel_hi:[1,1,0]
	v_exp_f32_e32 v236, v236
	v_exp_f32_e32 v237, v237
	v_exp_f32_e32 v238, v238
	v_exp_f32_e32 v239, v239
	v_exp_f32_e32 v240, v240
	v_exp_f32_e32 v241, v241
	v_exp_f32_e32 v242, v242
	v_exp_f32_e32 v243, v243
	v_exp_f32_e32 v244, v244
	v_exp_f32_e32 v245, v245
	v_exp_f32_e32 v246, v246
	v_exp_f32_e32 v247, v247
	v_exp_f32_e32 v248, v248
	v_exp_f32_e32 v249, v249
	v_pk_add_f32 v[86:87], v[236:237], v[238:239]
	v_pk_add_f32 v[88:89], v[240:241], v[242:243]
	v_pk_add_f32 v[90:91], v[244:245], v[246:247]
	v_pk_mul_f32 v[92:93], v[236:237], v[192:193]
	v_pk_mul_f32 v[94:95], v[238:239], v[194:195]
	v_pk_add_f32 v[86:87], v[86:87], v[248:249]
	v_pk_add_f32 v[88:89], v[88:89], v[90:91]
	v_pk_fma_f32 v[92:93], v[240:241], v[196:197], v[92:93]
	v_pk_fma_f32 v[94:95], v[242:243], v[198:199], v[94:95]
	v_pk_add_f32 v[86:87], v[86:87], v[88:89]
	v_pk_fma_f32 v[92:93], v[244:245], v[200:201], v[92:93]
	v_pk_fma_f32 v[94:95], v[246:247], v[202:203], v[94:95]
	v_add_f32_e32 v86, v86, v87
	v_pk_fma_f32 v[92:93], v[248:249], v[204:205], v[92:93]
	v_rcp_f32_e32 v87, v86
	v_pk_add_f32 v[92:93], v[92:93], v[94:95]
	v_mul_f32_e32 v87, v55, v87
	v_add_f32_e32 v92, v92, v93
	v_mul_f32_e32 v109, v86, v87
	v_mul_f32_e32 v92, v92, v87
	v_mul_f32_e32 v102, 0x43800000, v87
	v_mul_f32_e32 v106, 0x3d800000, v92
	v_max3_f32 v122, v103, v105, v106
	v_cmp_gt_u32_e64 s[6:7], 16, v104
	v_mov_b32_e32 v123, v122
	s_nop 1
	v_permlane16_swap_b32_e32 v122, v123
	v_max_f32_e32 v122, v122, v123
	v_mov_b32_e32 v123, v122
	s_nop 1
	v_permlane32_swap_b32_e32 v122, v123
	v_max_f32_e32 v36, v122, v123
	v_mul_f32_e32 v123, 0x3fb8aa3b, v36
	v_fma_f32 v111, v103, v121, -v123
	v_exp_f32_e32 v111, v111
	s_nop 0
	v_mul_f32_e32 v112, v111, v100
	v_mul_f32_e32 v110, v111, v107
	v_mov_b32_e32 v114, v111
	v_pk_mul_f32 v[208:209], v[208:209], v[112:113] op_sel_hi:[1,0]
	v_pk_mul_f32 v[210:211], v[210:211], v[112:113] op_sel_hi:[1,0]
	v_pk_mul_f32 v[212:213], v[212:213], v[112:113] op_sel_hi:[1,0]
	v_pk_mul_f32 v[214:215], v[214:215], v[112:113] op_sel_hi:[1,0]
	v_pk_mul_f32 v[216:217], v[216:217], v[112:113] op_sel_hi:[1,0]
	v_pk_mul_f32 v[218:219], v[218:219], v[112:113] op_sel_hi:[1,0]
	v_pk_mul_f32 v[220:221], v[220:221], v[112:113] op_sel_hi:[1,0]
	s_waitcnt vmcnt(13)
	v_mov_b32_e32 v115, v110
	v_fma_mix_f32 v116, v110, v70, 0 op_sel_hi:[0,1,0]
	v_fma_mix_f32 v117, v110, v70, 0 op_sel:[0,1,0] op_sel_hi:[0,1,0]
	v_fma_mix_f32 v118, v110, v71, 0 op_sel_hi:[0,1,0]
	v_cvt_pk_fp8_f32 v72, v208, v209
	v_cvt_pk_fp8_f32 v73, v212, v213
	v_cvt_pk_fp8_f32 v74, v216, v217
	v_cvt_pk_fp8_f32 v75, v220, v221
	v_cvt_pk_fp8_f32 v72, v210, v211 op_sel:[0,0,1]
	v_cvt_pk_fp8_f32 v73, v214, v215 op_sel:[0,0,1]
	v_cvt_pk_fp8_f32 v74, v218, v219 op_sel:[0,0,1]
	s_nop 1
	v_mfma_f32_16x16x32_fp8_fp8 v[152:155], v[72:73], v[30:31], 0
	v_mfma_f32_16x16x32_fp8_fp8 v[152:155], v[74:75], v[32:33], v[152:155]
	v_fma_f32 v111, v105, v121, -v123
	v_exp_f32_e32 v111, v111
	s_nop 0
	v_mul_f32_e32 v112, v111, v101
	v_mul_f32_e32 v110, v111, v108
	v_add_f32_e32 v114, v114, v111
	v_pk_mul_f32 v[222:223], v[222:223], v[112:113] op_sel_hi:[1,0]
	v_pk_mul_f32 v[224:225], v[224:225], v[112:113] op_sel_hi:[1,0]
	v_pk_mul_f32 v[226:227], v[226:227], v[112:113] op_sel_hi:[1,0]
	v_pk_mul_f32 v[228:229], v[228:229], v[112:113] op_sel_hi:[1,0]
	v_pk_mul_f32 v[230:231], v[230:231], v[112:113] op_sel_hi:[1,0]
	v_pk_mul_f32 v[232:233], v[232:233], v[112:113] op_sel_hi:[1,0]
	v_pk_mul_f32 v[234:235], v[234:235], v[112:113] op_sel_hi:[1,0]
	s_waitcnt vmcnt(11)
	v_add_f32_e32 v115, v115, v110
	v_fma_mix_f32 v116, v110, v66, v116 op_sel_hi:[0,1,0]
	v_fma_mix_f32 v117, v110, v66, v117 op_sel:[0,1,0] op_sel_hi:[0,1,0]
	v_fma_mix_f32 v118, v110, v67, v118 op_sel_hi:[0,1,0]
	v_cvt_pk_fp8_f32 v76, v222, v223
	v_cvt_pk_fp8_f32 v77, v226, v227
	v_cvt_pk_fp8_f32 v78, v230, v231
	v_cvt_pk_fp8_f32 v79, v234, v235
	v_cvt_pk_fp8_f32 v76, v224, v225 op_sel:[0,0,1]
	v_cvt_pk_fp8_f32 v77, v228, v229 op_sel:[0,0,1]
	v_cvt_pk_fp8_f32 v78, v232, v233 op_sel:[0,0,1]
	s_nop 1
	v_mfma_f32_16x16x32_fp8_fp8 v[152:155], v[76:77], v[26:27], v[152:155]
	v_mfma_f32_16x16x32_fp8_fp8 v[152:155], v[78:79], v[28:29], v[152:155]
	v_fma_f32 v111, v106, v121, -v123
	v_exp_f32_e32 v111, v111
	s_nop 0
	v_mul_f32_e32 v112, v111, v102
	v_mul_f32_e32 v110, v111, v109
	v_add_f32_e32 v114, v114, v111
	v_pk_mul_f32 v[236:237], v[236:237], v[112:113] op_sel_hi:[1,0]
	v_pk_mul_f32 v[238:239], v[238:239], v[112:113] op_sel_hi:[1,0]
	v_pk_mul_f32 v[240:241], v[240:241], v[112:113] op_sel_hi:[1,0]
	v_pk_mul_f32 v[242:243], v[242:243], v[112:113] op_sel_hi:[1,0]
	v_pk_mul_f32 v[244:245], v[244:245], v[112:113] op_sel_hi:[1,0]
	v_pk_mul_f32 v[246:247], v[246:247], v[112:113] op_sel_hi:[1,0]
	v_pk_mul_f32 v[248:249], v[248:249], v[112:113] op_sel_hi:[1,0]
	s_waitcnt vmcnt(9)
	v_add_f32_e32 v115, v115, v110
	v_fma_mix_f32 v116, v110, v68, v116 op_sel_hi:[0,1,0]
	v_fma_mix_f32 v117, v110, v68, v117 op_sel:[0,1,0] op_sel_hi:[0,1,0]
	v_fma_mix_f32 v118, v110, v69, v118 op_sel_hi:[0,1,0]
	v_cvt_pk_fp8_f32 v80, v236, v237
	v_cvt_pk_fp8_f32 v81, v240, v241
	v_cvt_pk_fp8_f32 v82, v244, v245
	v_cvt_pk_fp8_f32 v83, v248, v249
	v_cvt_pk_fp8_f32 v80, v238, v239 op_sel:[0,0,1]
	v_cvt_pk_fp8_f32 v81, v242, v243 op_sel:[0,0,1]
	v_cvt_pk_fp8_f32 v82, v246, v247 op_sel:[0,0,1]
	s_nop 1
	v_mfma_f32_16x16x32_fp8_fp8 v[152:155], v[80:81], v[18:19], v[152:155]
	v_mfma_f32_16x16x32_fp8_fp8 v[152:155], v[82:83], v[20:21], v[152:155]
	v_mov_b32_e32 v86, v114
	v_mov_b32_e32 v87, v115
	v_mov_b32_e32 v88, v116
	v_mov_b32_e32 v89, v117
	v_mov_b32_e32 v90, v118
	v_permlane16_swap_b32_e32 v114, v86
	v_permlane16_swap_b32_e32 v115, v87
	v_permlane16_swap_b32_e32 v116, v88
	v_permlane16_swap_b32_e32 v117, v89
	v_permlane16_swap_b32_e32 v118, v90
	v_add_f32_e32 v114, v114, v86
	v_add_f32_e32 v115, v115, v87
	v_add_f32_e32 v116, v116, v88
	v_add_f32_e32 v117, v117, v89
	v_add_f32_e32 v118, v118, v90
	v_mov_b32_e32 v86, v114
	v_mov_b32_e32 v87, v115
	v_mov_b32_e32 v88, v116
	v_mov_b32_e32 v89, v117
	v_mov_b32_e32 v90, v118
	v_permlane32_swap_b32_e32 v114, v86
	v_permlane32_swap_b32_e32 v115, v87
	v_permlane32_swap_b32_e32 v116, v88
	v_permlane32_swap_b32_e32 v117, v89
	v_permlane32_swap_b32_e32 v118, v90
	v_add_f32_e32 v37, v114, v86
	v_add_f32_e32 v20, v115, v87
	v_add_f32_e32 v18, v116, v88
	v_add_f32_e32 v19, v117, v89
	v_add_f32_e32 v21, v118, v90
	ds_write2_b32 v156, v152, v153 offset0:0 offset1:20
	ds_write2_b32 v156, v154, v155 offset0:40 offset1:60
